# same two-poll grid barrier wait, with the give-up bound raised to the original's order (0x40000 rounds)
# baseline (speedup 1.0000x reference)
.Lxb_spin_0:
	global_load_dword v4, v87, s[6:7] sc1
	s_waitcnt vmcnt(1)
	v_cmp_le_u32_e32 vcc, v5, v2
	s_cbranch_vccnz .Lxb_done_0
	global_load_dword v2, v87, s[6:7] sc1
	s_waitcnt vmcnt(1)
	v_cmp_le_u32_e32 vcc, v5, v4
	s_cbranch_vccnz .Lxb_done_0
	s_add_i32 s8, s8, 1
	s_cmp_lt_u32 s8, 0x40000
	s_cbranch_scc1 .Lxb_spin_0
